# speedup vs baseline: 1.0033x; 1.0033x over previous
_Z12giou_partialPK15HIP_vector_typeIfLj4EES2_S2_PKiPS_IfLj2EE:
	s_load_dwordx8 s[16:23], s[0:1], 0x0
	s_load_dwordx2 s[24:25], s[0:1], 0x20
	s_movk_i32 s3, 0x200
	s_lshl_b32 s6, s2, 9
	v_cmp_gt_u32_e32 vcc, s3, v0
	v_lshlrev_b32_e32 v11, 4, v0
	v_lshrrev_b32_e32 v1, 6, v0
	v_and_b32_e32 v10, 63, v0
	v_lshl_add_u32 v6, v1, 18, s6
	v_lshlrev_b32_e32 v8, 2, v6
	v_lshl_add_u32 v8, v10, 4, v8
	s_lshl_b32 s7, s2, 13
	v_readfirstlane_b32 s15, v1
	s_waitcnt lgkmcnt(0)
	s_add_u32 s20, s20, s7
	s_addc_u32 s21, s21, 0
	global_load_dwordx4 v[12:15], v8, s[22:23] nt
	global_load_dwordx4 v[16:19], v8, s[22:23] offset:1024 nt
	s_and_saveexec_b64 s[8:9], vcc
	s_cbranch_execz .Lno_anc
	global_load_dwordx4 v[2:5], v11, s[20:21] nt
.Lno_anc:
	s_or_b64 exec, exec, s[8:9]
	v_mov_b32_e32 v7, 0x80
	s_waitcnt vmcnt(0)
	v_cmp_ne_u32_e64 s[4:5], 0, v12
	s_nop 1
	v_cndmask_b32_e64 v8, 0, 1, s[4:5]
	v_cmp_eq_u32_e64 s[4:5], 0, v13
	s_nop 1
	v_cndmask_b32_e64 v9, 2, 0, s[4:5]
	v_cmp_eq_u32_e64 s[4:5], 0, v14
	v_or_b32_e32 v8, v9, v8
	s_nop 0
	v_cndmask_b32_e64 v12, 4, 0, s[4:5]
	v_cmp_eq_u32_e64 s[4:5], 0, v15
	s_nop 1
	v_cndmask_b32_e64 v13, 8, 0, s[4:5]
	v_cmp_eq_u32_e64 s[4:5], 0, v16
	v_or3_b32 v8, v8, v12, v13
	s_nop 0
	v_cndmask_b32_e64 v14, 16, 0, s[4:5]
	v_cmp_eq_u32_e64 s[4:5], 0, v17
	s_nop 1
	v_cndmask_b32_e64 v15, 32, 0, s[4:5]
	v_cmp_eq_u32_e64 s[4:5], 0, v18
	s_nop 1
	v_cndmask_b32_e64 v16, 64, 0, s[4:5]
	v_cmp_eq_u32_e64 s[4:5], 0, v19
	s_nop 1
	v_cndmask_b32_e64 v7, v7, 0, s[4:5]
	v_or_b32_e32 v7, v16, v7
	v_or3_b32 v9, v7, v15, v14
	v_or_b32_e32 v7, v9, v8
	v_bcnt_u32_b32 v8, v8, 0
	v_bcnt_u32_b32 v9, v9, 0
	v_lshl_or_b32 v9, v9, 16, v8
	v_cmp_ne_u32_e64 s[4:5], 0, v7
	s_nop 0
	v_add_u32_dpp v8, v9, v9 row_shr:1 row_mask:0xf bank_mask:0xf bound_ctrl:1
	s_nop 1
	v_add_u32_dpp v8, v8, v8 row_shr:2 row_mask:0xf bank_mask:0xf bound_ctrl:1
	s_nop 1
	v_add_u32_dpp v8, v8, v8 row_shr:4 row_mask:0xf bank_mask:0xf bound_ctrl:1
	s_nop 1
	v_add_u32_dpp v12, v8, v8 row_shr:8 row_mask:0xf bank_mask:0xf bound_ctrl:1
	s_nop 1
	v_add_u32_dpp v12, v12, v12 row_bcast:15 row_mask:0xa bank_mask:0xf
	s_nop 1
	v_add_u32_dpp v12, v12, v12 row_bcast:31 row_mask:0xc bank_mask:0xf
	s_nop 0
	v_readlane_b32 s14, v12, 63
	s_and_b32 s3, s14, 0xffff
	s_and_saveexec_b64 s[10:11], s[4:5]
	s_cbranch_execz .LBB0_5
	v_sub_u32_e32 v12, v12, v9
	v_lshlrev_b32_e32 v8, 10, v1
	v_add_u32_sdwa v9, sext(v12), s3 dst_sel:DWORD dst_unused:UNUSED_PAD src0_sel:WORD_1 src1_sel:DWORD
	v_and_b32_e32 v12, 0xffff, v12
	v_lshlrev_b32_e32 v13, 2, v10
	s_mov_b64 s[12:13], 0
	v_mov_b32_e32 v14, 0x100

.LBB0_5:
	s_or_b64 exec, exec, s[10:11]
	s_and_saveexec_b64 s[0:1], vcc
	ds_write_b128 v11, v[2:5] offset:16384
	s_or_b64 exec, exec, s[0:1]
	s_ashr_i32 s0, s14, 16
	s_add_i32 s3, s3, s0
	v_cmp_gt_i32_e32 vcc, s3, v10
	v_mov_b32_e32 v2, 0
	s_waitcnt lgkmcnt(0)
	s_and_saveexec_b64 s[0:1], vcc
	s_cbranch_execz .Lmid_bar
	v_lshlrev_b32_e32 v3, 1, v10
	v_lshl_or_b32 v3, v1, 10, v3
	v_mov_b32_e32 v4, v10
	ds_read_u16 v5, v3
	s_waitcnt lgkmcnt(0)
	v_add_u32_e32 v8, v6, v5
	v_lshlrev_b32_e32 v8, 4, v8
	global_load_dwordx4 v[12:15], v8, s[16:17] nt
	global_load_dwordx4 v[16:19], v8, s[18:19] nt
	v_lshlrev_b32_e32 v5, 4, v5
.Lmid_bar:
	s_barrier
	s_cbranch_execz .Lgather_done
.Lgather_loop:
	ds_read_b128 v[20:23], v5 offset:16384
	s_waitcnt lgkmcnt(0)
	v_pk_add_f32 v[8:9], v[22:23], v[20:21] neg_lo:[0,1] neg_hi:[0,1]
	s_nop 0
	v_pk_fma_f32 v[20:21], v[8:9], 0.5, v[20:21] op_sel_hi:[1,0,1]
	s_waitcnt vmcnt(1)
	v_mul_f32_e32 v5, 0x3fb8aa3b, v14
	v_mul_f32_e32 v7, 0x3fb8aa3b, v15
	v_pk_fma_f32 v[12:13], v[12:13], v[8:9], v[20:21]
	s_waitcnt vmcnt(0)
	v_sub_f32_e32 v14, v18, v16
	v_sub_f32_e32 v20, v19, v17
	v_max_f32_e32 v11, v18, v18
	v_max_f32_e32 v15, v16, v16
	v_max_f32_e32 v18, v19, v19
	v_max_f32_e32 v19, v17, v17
	v_exp_f32_e32 v16, v5
	v_exp_f32_e32 v17, v7
	s_nop 0
	v_pk_mul_f32 v[8:9], v[16:17], v[8:9]
	s_nop 0
	v_pk_fma_f32 v[16:17], v[8:9], 0.5, v[12:13] op_sel_hi:[1,0,1] neg_lo:[1,0,0] neg_hi:[1,0,0]
	v_pk_fma_f32 v[8:9], v[8:9], 0.5, v[12:13] op_sel_hi:[1,0,1]
	v_max_f32_e32 v7, v16, v15
	v_min_f32_e32 v5, v8, v11
	v_min_f32_e32 v21, v9, v18
	v_max_f32_e32 v22, v17, v19
	v_pk_add_f32 v[12:13], v[8:9], v[16:17] neg_lo:[0,1] neg_hi:[0,1]
	v_max_f32_e32 v8, v8, v11
	v_min_f32_e32 v11, v16, v15
	v_max_f32_e32 v9, v9, v18
	v_min_f32_e32 v15, v17, v19
	v_sub_f32_e32 v5, v5, v7
	v_sub_f32_e32 v7, v21, v22
	v_sub_f32_e32 v8, v8, v11
	v_sub_f32_e32 v9, v9, v15
	v_max_f32_e32 v15, 0, v5
	v_max_f32_e32 v21, 0, v7
	v_max_f32_e32 v5, 0, v8
	v_max_f32_e32 v7, 0, v9
	v_pk_mul_f32 v[8:9], v[14:15], v[20:21]
	v_mul_f32_e32 v11, v5, v7
	v_fma_f32 v8, v12, v13, v8
	v_sub_f32_e32 v8, v8, v9
	v_rcp_f32_e32 v14, v11
	v_rcp_f32_e32 v15, v8
	v_fma_f32 v8, v5, v7, -v8
	v_pk_mul_f32 v[8:9], v[14:15], v[8:9]
	s_nop 0
	v_sub_f32_e32 v5, v8, v9
	v_add_f32_e32 v5, 1.0, v5
	v_add_f32_e32 v2, v2, v5
	v_add_u32_e32 v4, 64, v4
	v_add_u32_e32 v3, 0x80, v3
	v_cmp_gt_i32_e32 vcc, s3, v4
	s_and_b64 exec, exec, vcc
	s_cbranch_execz .Lgather_done
	ds_read_u16 v5, v3
	s_waitcnt lgkmcnt(0)
	v_add_u32_e32 v8, v6, v5
	v_lshlrev_b32_e32 v8, 4, v8
	global_load_dwordx4 v[12:15], v8, s[16:17] nt
	global_load_dwordx4 v[16:19], v8, s[18:19] nt
	v_lshlrev_b32_e32 v5, 4, v5
	s_branch .Lgather_loop
.Lgather_done:
	s_mov_b64 exec, -1
	v_add_f32_dpp v2, v2, v2 quad_perm:[1,0,3,2] row_mask:0xf bank_mask:0xf bound_ctrl:1
	s_nop 1
	v_add_f32_dpp v2, v2, v2 quad_perm:[2,3,0,1] row_mask:0xf bank_mask:0xf bound_ctrl:1
	s_nop 1
	v_add_f32_dpp v2, v2, v2 row_half_mirror row_mask:0xf bank_mask:0xf bound_ctrl:1
	s_nop 1
	v_add_f32_dpp v2, v2, v2 row_mirror row_mask:0xf bank_mask:0xf bound_ctrl:1
	s_nop 1
	v_add_f32_dpp v2, v2, v2 row_bcast:15 row_mask:0xa bank_mask:0xf
	s_nop 1
	v_add_f32_dpp v2, v2, v2 row_bcast:31 row_mask:0xc bank_mask:0xf
	s_nop 0
	v_readlane_b32 s4, v2, 63
	v_cvt_f32_i32_e32 v3, s3
	v_lshlrev_b32_e32 v4, 3, v1
	s_mov_b64 exec, 1
	v_mov_b32_e32 v2, s4
	ds_write_b64 v4, v[2:3] offset:24576
	s_mov_b64 exec, -1
	s_waitcnt lgkmcnt(0)
	s_barrier
	s_cmp_lg_u32 s15, 0
	s_cbranch_scc1 .Lpartial_end
	v_and_b32_e32 v4, 15, v10
	v_lshlrev_b32_e32 v4, 3, v4
	ds_read_b64 v[2:3], v4 offset:24576
	s_lshl_b32 s0, s2, 3
	v_mov_b32_e32 v5, s0
	s_waitcnt lgkmcnt(0)
	v_add_f32_dpp v2, v2, v2 quad_perm:[1,0,3,2] row_mask:0xf bank_mask:0xf bound_ctrl:1
	v_add_f32_dpp v3, v3, v3 quad_perm:[1,0,3,2] row_mask:0xf bank_mask:0xf bound_ctrl:1
	s_nop 0
	v_add_f32_dpp v2, v2, v2 quad_perm:[2,3,0,1] row_mask:0xf bank_mask:0xf bound_ctrl:1
	v_add_f32_dpp v3, v3, v3 quad_perm:[2,3,0,1] row_mask:0xf bank_mask:0xf bound_ctrl:1
	s_nop 0
	v_add_f32_dpp v2, v2, v2 row_half_mirror row_mask:0xf bank_mask:0xf bound_ctrl:1
	v_add_f32_dpp v3, v3, v3 row_half_mirror row_mask:0xf bank_mask:0xf bound_ctrl:1
	s_nop 0
	v_add_f32_dpp v2, v2, v2 row_mirror row_mask:0xf bank_mask:0xf bound_ctrl:1
	v_add_f32_dpp v3, v3, v3 row_mirror row_mask:0xf bank_mask:0xf bound_ctrl:1
	s_mov_b64 exec, 1
	global_store_dwordx2 v5, v[2:3], s[24:25]

	.amdhsa_kernel _Z12giou_partialPK15HIP_vector_typeIfLj4EES2_S2_PKiPS_IfLj2EE
		.amdhsa_group_segment_fixed_size 24704
		.amdhsa_private_segment_fixed_size 0
		.amdhsa_kernarg_size 40
		.amdhsa_user_sgpr_count 2
		.amdhsa_user_sgpr_dispatch_ptr 0
		.amdhsa_user_sgpr_queue_ptr 0
		.amdhsa_user_sgpr_kernarg_segment_ptr 1
		.amdhsa_user_sgpr_dispatch_id 0
		.amdhsa_user_sgpr_kernarg_preload_length 0
		.amdhsa_user_sgpr_kernarg_preload_offset 0
		.amdhsa_user_sgpr_private_segment_size 0
		.amdhsa_uses_dynamic_stack 0
		.amdhsa_enable_private_segment 0
		.amdhsa_system_sgpr_workgroup_id_x 1
		.amdhsa_system_sgpr_workgroup_id_y 0
		.amdhsa_system_sgpr_workgroup_id_z 0
		.amdhsa_system_sgpr_workgroup_info 0
		.amdhsa_system_vgpr_workitem_id 0
		.amdhsa_next_free_vgpr 24
		.amdhsa_next_free_sgpr 26
		.amdhsa_accum_offset 24
		.amdhsa_reserve_vcc 1
		.amdhsa_float_round_mode_32 0
		.amdhsa_float_round_mode_16_64 0
		.amdhsa_float_denorm_mode_32 3
		.amdhsa_float_denorm_mode_16_64 3
		.amdhsa_dx10_clamp 1
		.amdhsa_ieee_mode 1
		.amdhsa_fp16_overflow 0
		.amdhsa_tg_split 0
		.amdhsa_exception_fp_ieee_invalid_op 0
		.amdhsa_exception_fp_denorm_src 0
		.amdhsa_exception_fp_ieee_div_zero 0
		.amdhsa_exception_fp_ieee_overflow 0
		.amdhsa_exception_fp_ieee_underflow 0
		.amdhsa_exception_fp_ieee_inexact 0
		.amdhsa_exception_int_div_zero 0
	.end_amdhsa_kernel

.Lfunc_end0:
	.size	_Z12giou_partialPK15HIP_vector_typeIfLj4EES2_S2_PKiPS_IfLj2EE, .Lfunc_end0-_Z12giou_partialPK15HIP_vector_typeIfLj4EES2_S2_PKiPS_IfLj2EE
	.set _Z12giou_partialPK15HIP_vector_typeIfLj4EES2_S2_PKiPS_IfLj2EE.num_vgpr, 24
	.set _Z12giou_partialPK15HIP_vector_typeIfLj4EES2_S2_PKiPS_IfLj2EE.num_agpr, 0
	.set _Z12giou_partialPK15HIP_vector_typeIfLj4EES2_S2_PKiPS_IfLj2EE.numbered_sgpr, 26
	.set _Z12giou_partialPK15HIP_vector_typeIfLj4EES2_S2_PKiPS_IfLj2EE.num_named_barrier, 0
	.set _Z12giou_partialPK15HIP_vector_typeIfLj4EES2_S2_PKiPS_IfLj2EE.private_seg_size, 0
	.set _Z12giou_partialPK15HIP_vector_typeIfLj4EES2_S2_PKiPS_IfLj2EE.uses_vcc, 1
	.set _Z12giou_partialPK15HIP_vector_typeIfLj4EES2_S2_PKiPS_IfLj2EE.uses_flat_scratch, 0
	.set _Z12giou_partialPK15HIP_vector_typeIfLj4EES2_S2_PKiPS_IfLj2EE.has_dyn_sized_stack, 0
	.set _Z12giou_partialPK15HIP_vector_typeIfLj4EES2_S2_PKiPS_IfLj2EE.has_recursion, 0
	.set _Z12giou_partialPK15HIP_vector_typeIfLj4EES2_S2_PKiPS_IfLj2EE.has_indirect_call, 0

amdhsa.kernels:
  - .agpr_count:     0
    .args:
      - .actual_access:  read_only
        .address_space:  global
        .offset:         0
        .size:           8
        .value_kind:     global_buffer
      - .actual_access:  read_only
        .address_space:  global
        .offset:         8
        .size:           8
        .value_kind:     global_buffer
      - .actual_access:  read_only
        .address_space:  global
        .offset:         16
        .size:           8
        .value_kind:     global_buffer
      - .actual_access:  read_only
        .address_space:  global
        .offset:         24
        .size:           8
        .value_kind:     global_buffer
      - .actual_access:  write_only
        .address_space:  global
        .offset:         32
        .size:           8
        .value_kind:     global_buffer
    .group_segment_fixed_size: 24704
    .kernarg_segment_align: 8
    .kernarg_segment_size: 40
    .language:       OpenCL C
    .language_version:
      - 2
      - 0
    .max_flat_workgroup_size: 1024
    .name:           _Z12giou_partialPK15HIP_vector_typeIfLj4EES2_S2_PKiPS_IfLj2EE
    .private_segment_fixed_size: 0
    .sgpr_count:     32
    .sgpr_spill_count: 0
    .symbol:         _Z12giou_partialPK15HIP_vector_typeIfLj4EES2_S2_PKiPS_IfLj2EE.kd
    .uniform_work_group_size: 1
    .uses_dynamic_stack: false
    .vgpr_count:     24
    .vgpr_spill_count: 0
    .wavefront_size: 64
  - .agpr_count:     0
    .args:
      - .actual_access:  read_only
        .address_space:  global
        .offset:         0
        .size:           8
        .value_kind:     global_buffer
      - .actual_access:  write_only
        .address_space:  global
        .offset:         8
        .size:           8
        .value_kind:     global_buffer
    .group_segment_fixed_size: 0
    .kernarg_segment_align: 8
    .kernarg_segment_size: 16
    .language:       OpenCL C
    .language_version:
      - 2
      - 0
    .max_flat_workgroup_size: 64
    .name:           _Z10giou_finalPK15HIP_vector_typeIfLj2EEPf
    .private_segment_fixed_size: 0
    .sgpr_count:     18
    .sgpr_spill_count: 0
    .symbol:         _Z10giou_finalPK15HIP_vector_typeIfLj2EEPf.kd
    .uniform_work_group_size: 1
    .uses_dynamic_stack: false
    .vgpr_count:     18
    .vgpr_spill_count: 0
    .wavefront_size: 64
